# on top of the XCD-contiguous MoE order: phase 9's multiply-first half chosen by blockIdx bit 7 instead of bit 3 (4x4 instead of 2x8 concurrent tiles per XCD)
# baseline (speedup 1.0000x reference)
.LBB0_6:
	s_ashr_i32 s3, s2, 31
	s_lshr_b32 s0, s3, 29
	s_add_i32 s5, s2, s0
	s_and_b32 s0, s5, -8
	s_sub_i32 s18, s2, s0
	s_lshl_b32 s0, s18, 4
	s_cmp_lt_i32 s18, 0
	s_mul_i32 s1, s18, 17
	s_cselect_b32 s0, s1, s0
	s_lshl_b32 s1, s18, 7
	s_cmp_lt_i32 s18, 0
	s_mul_i32 s4, s18, 0x81
	s_cselect_b32 s1, s4, s1
	s_lshl_b32 s4, s18, 6
	s_cmp_lt_i32 s18, 0
	s_movk_i32 s6, 0xc1
	s_mul_i32 s7, s18, 0x41
	s_movk_i32 s9, 0x181
	s_cselect_b32 s6, s6, 0xc0
	s_cselect_b32 s9, s9, 0x180
	s_cselect_b32 s4, s7, s4
	s_lshl_b32 s11, s2, 3
	s_lshl_b32 s7, s2, 9
	s_cmp_eq_u32 s8, 15
	v_writelane_b32 v253, s7, 6
	s_cselect_b64 s[12:13], -1, 0
	v_writelane_b32 v253, s12, 7
	s_cmp_eq_u32 s8, 14
	v_mov_b32_e32 v35, 0
	v_writelane_b32 v253, s13, 8
	s_cselect_b64 s[12:13], -1, 0
	v_writelane_b32 v253, s12, 9
	s_cmp_eq_u32 s8, 13
	s_mov_b32 s59, 0x20000
	v_writelane_b32 v253, s13, 10
	s_cselect_b64 s[12:13], -1, 0
	v_writelane_b32 v253, s12, 11
	s_cmp_eq_u32 s8, 12
	v_mbcnt_lo_u32_b32 v1, -1, 0
	v_writelane_b32 v253, s13, 12
	s_cselect_b64 s[12:13], -1, 0
	v_writelane_b32 v253, s12, 13
	s_cmp_eq_u32 s8, 11
	v_mov_b32_e32 v214, 0x358637bd
	v_writelane_b32 v253, s13, 14
	s_cselect_b64 s[12:13], -1, 0
	v_writelane_b32 v253, s12, 15
	s_cmp_eq_u32 s8, 10
	v_mov_b32_e32 v215, 1
	v_writelane_b32 v253, s13, 16
	s_cselect_b64 s[12:13], -1, 0
	v_writelane_b32 v253, s12, 17
	s_cmp_eq_u32 s8, 9
	s_movk_i32 s66, 0x4800
	v_writelane_b32 v253, s13, 18
	s_cselect_b64 s[12:13], -1, 0
	v_writelane_b32 v253, s12, 19
	s_cmp_eq_u32 s8, 8
	s_mov_b32 s67, s59
	v_writelane_b32 v253, s13, 20
	s_cselect_b64 s[12:13], -1, 0
	v_writelane_b32 v253, s12, 21
	s_cmp_eq_u32 s8, 7
	s_mov_b32 s58, 0x4f700000
	v_writelane_b32 v253, s13, 22
	s_cselect_b64 s[12:13], -1, 0
	v_writelane_b32 v253, s12, 23
	s_cmp_eq_u32 s8, 6
	v_mov_b32_e32 v216, 0x3a27c5ac
	v_writelane_b32 v253, s13, 24
	s_cselect_b64 s[12:13], -1, 0
	v_writelane_b32 v253, s12, 25
	s_cmp_eq_u32 s8, 5
	v_mov_b32_e32 v234, v35
	v_writelane_b32 v253, s13, 26
	s_cselect_b64 s[12:13], -1, 0
	v_writelane_b32 v253, s12, 27
	s_cmp_eq_u32 s8, 4
	v_mov_b32_e32 v235, v35
	v_writelane_b32 v253, s13, 28
	s_cselect_b64 s[12:13], -1, 0
	v_writelane_b32 v253, s12, 29
	s_cmp_eq_u32 s8, 3
	v_mov_b32_e32 v236, v35
	v_writelane_b32 v253, s13, 30
	s_cselect_b64 s[12:13], -1, 0
	v_writelane_b32 v253, s12, 31
	s_cmp_eq_u32 s8, 2
	v_mov_b32_e32 v237, v35
	v_writelane_b32 v253, s13, 32
	s_cselect_b64 s[12:13], -1, 0
	v_writelane_b32 v253, s12, 33
	s_cmp_eq_u32 s8, 1
	v_mov_b32_e32 v217, 2
	v_writelane_b32 v253, s13, 34
	s_cselect_b64 s[12:13], -1, 0
	v_writelane_b32 v253, s12, 35
	s_cmp_eq_u32 s8, 0
	v_mbcnt_hi_u32_b32 v218, -1, v1
	v_writelane_b32 v253, s13, 36
	s_cselect_b64 s[12:13], -1, 0
	v_writelane_b32 v253, s12, 37
	s_lshl_b32 s7, s8, 6
	s_cmpk_lt_i32 s2, 0xc00
	v_writelane_b32 v253, s13, 38
	v_writelane_b32 v253, s7, 39
	s_cselect_b64 s[12:13], -1, 0
	s_ashr_i32 s8, s5, 3
	v_writelane_b32 v253, s12, 40
	s_cmpk_lt_i32 s2, 0x600
	s_mul_i32 s5, s6, s18
	v_writelane_b32 v253, s13, 41
	s_cselect_b64 s[12:13], -1, 0
	s_add_i32 s5, s5, s8
	s_mul_hi_i32 s6, s5, 0x2aaaaaab
	s_lshr_b32 s7, s6, 31
	s_ashr_i32 s6, s6, 3
	s_add_i32 s6, s6, s7
	s_mul_i32 s7, s6, 48
	s_sub_i32 s5, s5, s7
	s_bfe_i32 s7, s5, 0x80000
	s_bfe_u32 s7, s7, 0x2000d
	s_add_i32 s7, s5, s7
	s_bfe_i32 s10, s7, 0x80000
	s_and_b32 s7, s7, 0xfc
	s_sub_i32 s5, s5, s7
	s_lshl_b32 s6, s6, 2
	s_sext_i32_i8 s5, s5
	v_writelane_b32 v253, s12, 42
	s_add_i32 s14, s6, s5
	s_mov_b32 s6, s14
	v_writelane_b32 v253, s13, 43
	s_ashr_i32 s15, s14, 31
	v_writelane_b32 v253, s6, 44
	s_sext_i32_i16 s10, s10
	s_ashr_i32 s16, s10, 4
	v_writelane_b32 v253, s7, 45
	s_lshl_b64 s[6:7], s[14:15], 19
	v_writelane_b32 v253, s6, 46
	s_lshl_b32 s5, s16, 9
	s_ashr_i32 s17, s16, 31
	v_writelane_b32 v253, s7, 47
	v_writelane_b32 v253, s5, 48
	s_ashr_i32 s5, s5, 31
	v_writelane_b32 v253, s5, 49
	s_mov_b32 s6, s16
	v_writelane_b32 v253, s6, 50
	s_ashr_i32 s12, s10, 2
	s_lshl_b32 s5, s12, 17
	v_writelane_b32 v253, s7, 51
	s_lshl_b64 s[6:7], s[16:17], 19
	v_writelane_b32 v253, s6, 52
	s_and_b32 s5, s5, 0x60000
	s_cmpk_lt_i32 s2, 0x200
	v_writelane_b32 v253, s7, 53
	v_writelane_b32 v253, s12, 54
	v_writelane_b32 v253, s5, 55
	s_cselect_b64 s[6:7], -1, 0
	v_writelane_b32 v253, s6, 56
	s_cmp_lt_i32 s2, 32
	v_mov_b64_e32 v[200:201], 0xc00
	v_writelane_b32 v253, s7, 57
	s_cselect_b64 s[6:7], -1, 0
	s_cmp_gt_i32 s2, 31
	v_writelane_b32 v253, s6, 58
	s_cselect_b64 s[12:13], -1, 0
	v_mov_b64_e32 v[202:203], 0xbff
	v_writelane_b32 v253, s7, 59
	s_and_b64 s[6:7], s[12:13], exec
	s_cselect_b32 s5, s2, 0x800
	s_bitcmp1_b32 s2, 3
	s_cselect_b64 s[6:7], -1, 0
	v_writelane_b32 v253, s12, 60
	s_and_b64 s[94:95], s[12:13], s[6:7]
	s_cmpk_lt_i32 s11, 0x4000
	v_writelane_b32 v253, s13, 61
	s_cselect_b64 s[6:7], -1, 0
	s_cmpk_lt_u32 s5, 0x800
	v_writelane_b32 v253, s11, 62
	s_cselect_b64 s[10:11], -1, 0
	s_or_b64 s[6:7], s[6:7], s[10:11]
	v_writelane_b32 v253, s5, 63
	v_writelane_b32 v254, s6, 0
	s_mul_i32 s5, s2, 0x120000
	s_lshl_b32 s80, s2, 6
	v_writelane_b32 v254, s7, 1
	s_add_i32 s6, s5, 0x3c800000
	v_writelane_b32 v254, s6, 2
	s_add_i32 s6, s5, 0x3c804800
	v_writelane_b32 v254, s6, 3
	s_add_i32 s6, s5, 0x3c809000
	v_writelane_b32 v254, s6, 4
	s_add_i32 s6, s5, 0x3c80d800
	v_writelane_b32 v254, s6, 5
	s_add_i32 s6, s5, 0x3c812000
	v_writelane_b32 v254, s6, 6
	s_add_i32 s6, s5, 0x3c816800
	v_writelane_b32 v254, s6, 7
	s_add_i32 s6, s5, 0x3c81b000
	v_writelane_b32 v254, s6, 8
	s_add_i32 s6, s5, 0x3c81f800
	v_writelane_b32 v254, s6, 9
	s_add_i32 s6, s5, 0x3c824000
	v_writelane_b32 v254, s6, 10
	s_add_i32 s5, s5, 0x3c828800
	v_writelane_b32 v254, s5, 11
	s_lshl_b32 s5, s2, 21
	s_add_i32 s6, s5, 0x307fc800
	v_writelane_b32 v254, s6, 12
	s_add_i32 s6, s5, 0x307fd800
	v_writelane_b32 v254, s6, 13
	s_add_i32 s6, s5, 0x307fe800
	v_writelane_b32 v254, s6, 14
	s_add_i32 s6, s5, 0x307ff800
	v_writelane_b32 v254, s6, 15
	s_add_i32 s6, s5, 0x30800800
	v_writelane_b32 v254, s6, 16
	s_add_i32 s6, s5, 0x30801800
	v_writelane_b32 v254, s6, 17
	s_add_i32 s6, s5, 0x30802800
	v_writelane_b32 v254, s6, 18
	s_add_i32 s6, s5, 0x30803800
	s_add_i32 s82, s5, 0x307fb800
	v_writelane_b32 v254, s6, 19
	s_add_i32 s5, s5, 0x30804800
	s_ashr_i32 s81, s80, 31
	v_writelane_b32 v254, s5, 20
	s_lshl_b64 s[6:7], s[2:3], 18
	v_writelane_b32 v254, s6, 21
	s_cmpk_lt_i32 s2, 0x400
	s_mul_i32 s5, s18, s9
	v_writelane_b32 v254, s7, 22
	s_cselect_b64 s[6:7], -1, 0
	s_bfe_u32 s19, s2, 0x10007
	v_writelane_b32 v254, s6, 23
	s_cmpk_lt_i32 s2, 0x80
	v_not_b32_e32 v219, 63
	v_writelane_b32 v254, s7, 24
	s_cselect_b64 s[6:7], -1, 0
	v_writelane_b32 v254, s6, 25
	s_cmpk_gt_i32 s2, 0x7f
	v_not_b32_e32 v220, 31
	v_writelane_b32 v254, s7, 26
	s_cselect_b64 s[6:7], -1, 0
	s_cmpk_lt_i32 s2, 0x100
	s_cselect_b64 s[10:11], -1, 0
	s_add_i32 s5, s5, s8
	v_writelane_b32 v254, s10, 27
	s_mul_hi_i32 s9, s5, 0x2aaaaaab
	s_add_i32 s4, s4, s8
	v_writelane_b32 v254, s11, 28
	s_lshr_b32 s10, s9, 31
	s_ashr_i32 s9, s9, 4
	s_add_i32 s10, s9, s10
	s_mul_i32 s9, s10, 0x60
	s_sub_i32 s5, s5, s9
	s_bfe_i32 s9, s5, 0x80000
	s_bfe_u32 s9, s9, 0x2000d
	s_add_i32 s11, s5, s9
	s_and_b32 s9, s11, 0xfc
	s_sub_i32 s5, s5, s9
	s_ashr_i32 s9, s4, 31
	s_lshr_b32 s9, s9, 28
	s_add_i32 s12, s4, s9
	s_and_b32 s9, s12, 0xfff0
	s_sub_i32 s4, s4, s9
	s_bfe_i32 s9, s4, 0x80000
	s_bfe_u32 s9, s9, 0x2000d
	s_add_i32 s13, s4, s9
	s_and_b32 s9, s13, 0xfc
	s_add_i32 s1, s1, s8
	s_sub_i32 s4, s4, s9
	s_ashr_i32 s9, s1, 31
	s_lshr_b32 s9, s9, 27
	s_add_i32 s14, s1, s9
	s_and_b32 s9, s14, 0xffe0
	s_sub_i32 s1, s1, s9
	s_bfe_i32 s9, s1, 0x80000
	s_bfe_u32 s9, s9, 0x2000d
	s_add_i32 s15, s1, s9
	s_and_b32 s9, s15, 0xfc
	s_sub_i32 s16, s1, s9
	s_lshr_b32 s1, s3, 30
	s_add_i32 s1, s2, s1
	s_ashr_i32 s9, s1, 2
	v_writelane_b32 v254, s9, 29
	s_add_i32 s9, 0, 0x20000
	s_lshl_b32 s17, s8, 2
	s_and_b32 s1, s1, -4
	s_add_i32 s17, s9, s17
	v_writelane_b32 v254, s17, 30
	s_add_i32 s9, s9, s1
	v_writelane_b32 v254, s9, 31
	s_ashr_i32 s9, s8, 31
	s_sub_i32 s24, s2, s1
	s_add_i32 s26, s0, s8
	s_lshl_b64 s[0:1], s[8:9], 18
	v_writelane_b32 v254, s0, 32
	s_sext_i32_i8 s5, s5
	s_sext_i32_i8 s4, s4
	v_writelane_b32 v254, s1, 33
	s_bfe_i32 s1, s11, 0x80000
	s_lshl_b32 s0, s10, 2
	s_sext_i32_i16 s1, s1
	s_add_i32 s20, s0, s5
	s_ashr_i32 s0, s1, 2
	v_writelane_b32 v254, s0, 34
	s_lshr_b32 s0, s1, 2
	s_bfe_i64 s[0:1], s[0:1], 0x100000
	s_lshl_b64 s[0:1], s[0:1], 20
	v_writelane_b32 v254, s0, 35
	s_ashr_i32 s25, s24, 31
	s_mov_b32 s8, s19
	v_writelane_b32 v254, s1, 36
	s_ashr_i32 s0, s12, 4
	s_bfe_i32 s1, s13, 0x80000
	s_lshl_b32 s0, s0, 2
	s_sext_i32_i16 s1, s1
	s_add_i32 s22, s0, s4
	s_lshr_b32 s0, s1, 2
	s_ashr_i32 s5, s1, 2
	s_bfe_i64 s[0:1], s[0:1], 0x100000
	s_lshl_b64 s[0:1], s[0:1], 17
	v_writelane_b32 v254, s0, 37
	s_sext_i32_i8 s4, s16
	s_ashr_i32 s19, s18, 31
	v_writelane_b32 v254, s1, 38
	s_ashr_i32 s0, s14, 5
	s_bfe_i32 s1, s15, 0x80000
	s_lshl_b32 s0, s0, 2
	s_sext_i32_i16 s1, s1
	s_add_i32 s88, s0, s4
	s_lshr_b32 s0, s1, 2
	s_ashr_i32 s83, s1, 2
	s_bfe_i64 s[0:1], s[0:1], 0x100000
	s_lshl_b64 s[14:15], s[0:1], 19
	v_writelane_b32 v254, s14, 39
	s_lshl_b64 s[0:1], s[0:1], 20
	s_ashr_i32 s21, s20, 31
	v_writelane_b32 v254, s15, 40
	v_writelane_b32 v254, s0, 41
	s_ashr_i32 s23, s22, 31
	s_ashr_i32 s89, s88, 31
	v_writelane_b32 v254, s1, 42
	v_writelane_b32 v254, s5, 43
	s_lshl_b32 s0, s5, 9
	v_writelane_b32 v254, s0, 44
	s_ashr_i32 s0, s0, 31
	v_writelane_b32 v254, s0, 45
	s_mov_b32 s0, s24
	v_writelane_b32 v254, s0, 46
	s_ashr_i32 s27, s26, 31
	v_mov_b32_e32 v221, 0x7fc00000
	v_writelane_b32 v254, s1, 47
	s_lshl_b64 s[0:1], s[24:25], 20
	v_writelane_b32 v254, s0, 48
	v_mov_b32_e32 v222, 0x80
	v_mov_b32_e32 v223, 0xff800000
	v_writelane_b32 v254, s1, 49
	s_mov_b32 s0, s18
	v_writelane_b32 v254, s0, 50
	v_mov_b64_e32 v[204:205], 0x400
	v_mov_b64_e32 v[206:207], 0x3ff
	v_writelane_b32 v254, s1, 51
	s_lshl_b64 s[0:1], s[18:19], 18
	v_writelane_b32 v254, s0, 52
	v_mov_b64_e32 v[210:211], 0x7f
	s_movk_i32 s33, 0xc0
	v_writelane_b32 v254, s1, 53
	s_lshr_b32 s97, s93, 3
	s_and_b32 s96, s2, 7
	s_mul_i32 s96, s96, s97
	s_lshr_b32 s97, s2, 3
	s_add_i32 s96, s96, s97
	s_and_b32 s97, s93, 7
	s_cmp_eq_u32 s97, 0
	s_cselect_b32 s96, s96, s2
	v_writelane_b32 v252, s96, 47
	s_lshr_b32 s97, s96, 2
	v_writelane_b32 v254, s97, 29
	s_and_b32 s97, s96, -4
	s_add_i32 s97, s97, 0x20000
	v_writelane_b32 v254, s97, 31
	s_and_b32 s97, s96, 3
	v_writelane_b32 v254, s97, 46
	s_lshl_b32 s97, s97, 20
	v_writelane_b32 v254, s97, 48
	s_lshr_b32 s97, s96, 3
	s_lshl_b32 s97, s97, 2
	s_add_i32 s97, s97, 0x20000
	v_writelane_b32 v254, s97, 30
	s_lshr_b32 s97, s96, 3
	s_lshl_b32 s97, s97, 18
	v_writelane_b32 v254, s97, 32
	s_and_b32 s97, s96, 7
	v_writelane_b32 v254, s97, 50
	s_lshl_b32 s97, s97, 18
	v_writelane_b32 v254, s97, 52
	s_mov_b32 s97, 0
	v_writelane_b32 v254, s97, 47
	v_writelane_b32 v254, s97, 49
	v_writelane_b32 v254, s97, 51
	v_writelane_b32 v254, s97, 53
	v_writelane_b32 v254, s97, 33
	s_mov_b32 s0, s20
	v_writelane_b32 v254, s0, 54
	s_movk_i32 s72, 0x7fff
	s_movk_i32 s73, 0x1000
	v_writelane_b32 v254, s1, 55
	s_lshl_b64 s[0:1], s[20:21], 20
	v_writelane_b32 v254, s0, 56
	s_movk_i32 s90, 0x2000
	s_movk_i32 s91, 0x3000
	v_writelane_b32 v254, s1, 57
	s_mov_b32 s0, s22
	v_writelane_b32 v254, s0, 58
	s_mov_b32 s92, 0x34800000
	s_mov_b32 s97, 0
	v_writelane_b32 v254, s1, 59
	s_lshl_b64 s[0:1], s[22:23], 19
	v_writelane_b32 v254, s0, 60
	s_mov_b64 s[78:79], 0x80
	s_mov_b64 s[76:77], 0x8000000
	v_writelane_b32 v254, s1, 61
	s_lshl_b64 s[0:1], s[88:89], 19
	v_writelane_b32 v254, s0, 62
	s_nop 1
	v_writelane_b32 v254, s1, 63
	s_lshl_b64 s[0:1], s[88:89], 20
	v_writelane_b32 v252, s0, 0
	s_nop 1
	v_writelane_b32 v252, s1, 1
	s_mov_b32 s0, s26
	v_writelane_b32 v252, s0, 2
	s_nop 1
	v_writelane_b32 v252, s1, 3
	s_lshl_b64 s[0:1], s[26:27], 20
	v_writelane_b32 v252, s0, 4
	s_nop 1
	v_writelane_b32 v252, s1, 5
	s_xor_b64 s[0:1], s[94:95], -1
	v_writelane_b32 v252, s0, 6
	s_nop 1
	v_writelane_b32 v252, s1, 7
	s_add_u32 s0, s60, 0x1000
	v_writelane_b32 v252, s0, 8
	s_addc_u32 s0, s61, 0
	v_writelane_b32 v252, s0, 9
	s_xor_b64 s[0:1], s[6:7], -1
	v_writelane_b32 v252, s0, 10
	s_add_i32 s4, 0, 0x20600
	s_mov_b32 s6, 0x3ffff
	v_writelane_b32 v252, s1, 11
	s_lshl_b32 s0, s2, 4
	v_writelane_b32 v252, s0, 12
	s_lshl_b32 s0, s2, 7
	v_writelane_b32 v252, s0, 13
	s_or_b32 s0, s0, 1
	v_writelane_b32 v252, s0, 14
	s_lshl_b32 s0, s2, 5
	v_writelane_b32 v252, s0, 15
	s_lshl_b32 s0, s2, 8
	v_writelane_b32 v252, s0, 16
	s_add_i32 s0, 0, 0x24020
	v_writelane_b32 v252, s0, 17
	s_add_i32 s0, 0, 0x24024
	v_writelane_b32 v252, s0, 18
	v_writelane_b32 v252, s4, 19
	s_add_i32 s4, 0, 0x20800
	v_writelane_b32 v252, s4, 20
	s_add_i32 s4, 0, 0x20a00
	v_writelane_b32 v252, s4, 21
	s_lshl_b64 s[4:5], s[80:81], 2
	v_writelane_b32 v252, s4, 22
	s_mov_b32 s0, 0x24800000
	s_mov_b32 s1, 0x2c800000
	v_writelane_b32 v252, s5, 23
	s_load_dwordx2 s[4:5], s[84:85], 0x100
	v_writelane_b32 v252, s84, 24
	s_waitcnt lgkmcnt(0)
	s_mov_b32 s48, s4
	v_writelane_b32 v252, s85, 25
	v_writelane_b32 v252, s93, 26
	v_writelane_b32 v252, s86, 27
	s_nop 1
	v_writelane_b32 v252, s87, 28
	v_writelane_b32 v252, s80, 29
	s_nop 1
	v_writelane_b32 v252, s81, 30
	v_writelane_b32 v252, s82, 31
	v_writelane_b32 v252, s88, 32
	s_nop 1
	v_writelane_b32 v252, s89, 33
	v_writelane_b32 v252, s83, 34
	s_branch .LBB0_8
